# attention: guarded diagonal fast path (exact same-position scores for frames fq,fq+-1,fq+-2 + Cauchy-Schwarz bound on all other pairs; 3-term softmax in registers), full path kept as workgroup-uniform
# speedup vs baseline: 1.0512x; 1.0512x over previous
_Z8attn_fwdPKDF16_S0_S0_PKjPf:
	s_mov_b64 s[36:37], s[0:1]
	s_mov_b32 s38, s2
	s_load_dwordx4 s[8:11], s[0:1], 0x0
	s_load_dwordx4 s[12:15], s[0:1], 0x10
	s_load_dwordx2 s[16:17], s[0:1], 0x20
	s_lshl_b32 s3, s2, 1
	s_mul_hi_u32 s4, s2, 0xaaaaaaab
	s_and_b32 s3, s3, 14
	s_lshr_b32 s4, s4, 6
	s_add_i32 s6, s3, s4
	s_lshr_b32 s5, s2, 3
	s_mul_hi_u32 s7, s5, 0x15555556
	s_mul_i32 s7, s7, 12
	s_sub_i32 s20, s5, s7
	v_and_b32_e32 v1, 63, v0
	v_and_b32_e32 v2, 31, v0
	v_bfe_u32 v3, v0, 5, 1
	v_readfirstlane_b32 s19, v0
	s_nop 3
	s_lshr_b32 s19, s19, 6
	s_lshl_b32 s18, s19, 5
	v_or_b32_e32 v4, s18, v2
	v_lshlrev_b32_e32 v4, 7, v4
	v_lshl_or_b32 v4, v3, 4, v4
	v_mul_u32_u24_e32 v5, 0x1800, v1
	v_min_u32_e32 v6, 47, v1
	v_lshlrev_b32_e32 v6, 2, v6
	s_mul_i32 s21, s6, 0xc00
	s_cmp_lt_u32 s20, 11
	s_cselect_b32 s22, 1, 0
	s_cselect_b32 s40, 0, 0xf149f2ca
	s_add_i32 s22, s20, s22
	s_cmp_gt_u32 s20, 0
	s_cselect_b32 s23, 1, 0
	s_cselect_b32 s41, 0, 0xf149f2ca
	s_sub_i32 s23, s20, s23
	s_cmp_lt_u32 s20, 10
	s_cselect_b32 s24, 2, 0
	s_cselect_b32 s42, 0, 0xf149f2ca
	s_add_i32 s24, s20, s24
	s_cmp_gt_u32 s20, 1
	s_cselect_b32 s25, 2, 0
	s_cselect_b32 s43, 0, 0xf149f2ca
	s_sub_i32 s25, s20, s25
	s_waitcnt lgkmcnt(0)
	s_lshl_b32 s26, s20, 8
	s_add_i32 s26, s26, s21
	s_lshl_b32 s26, s26, 7
	s_add_u32 s44, s10, s26
	s_addc_u32 s45, s11, 0
	s_add_u32 s54, s8, s26
	s_addc_u32 s55, s9, 0
	s_lshl_b32 s27, s20, 8
	s_add_i32 s27, s27, s21
	s_add_i32 s27, s27, s18
	s_lshl_b32 s27, s27, 8
	s_add_u32 s62, s16, s27
	s_addc_u32 s63, s17, 0
	s_lshl_b32 s26, s22, 8
	s_add_i32 s26, s26, s21
	s_lshl_b32 s26, s26, 7
	s_add_u32 s46, s10, s26
	s_addc_u32 s47, s11, 0
	s_lshl_b32 s26, s23, 8
	s_add_i32 s26, s26, s21
	s_lshl_b32 s26, s26, 7
	s_add_u32 s48, s10, s26
	s_addc_u32 s49, s11, 0
	s_lshl_b32 s26, s24, 8
	s_add_i32 s26, s26, s21
	s_lshl_b32 s26, s26, 7
	s_add_u32 s50, s10, s26
	s_addc_u32 s51, s11, 0
	s_lshl_b32 s26, s25, 8
	s_add_i32 s26, s26, s21
	s_lshl_b32 s26, s26, 7
	s_add_u32 s52, s10, s26
	s_addc_u32 s53, s11, 0
	s_mul_i32 s28, s6, 0x30000
	s_add_i32 s28, s28, s18
	s_lshl_b32 s26, s20, 8
	s_add_i32 s26, s26, s28
	s_lshl_b32 s26, s26, 1
	s_add_u32 s56, s12, s26
	s_addc_u32 s57, s13, 0
	s_lshl_b32 s26, s22, 8
	s_add_i32 s26, s26, s28
	s_lshl_b32 s26, s26, 1
	s_add_u32 s58, s12, s26
	s_addc_u32 s59, s13, 0
	s_lshl_b32 s26, s23, 8
	s_add_i32 s26, s26, s28
	s_lshl_b32 s26, s26, 1
	s_add_u32 s60, s12, s26
	s_addc_u32 s61, s13, 0
	s_mul_i32 s26, s6, 0xc0
	s_add_u32 s64, s14, s26
	s_addc_u32 s65, s15, 0
	global_load_dword v7, v6, s[64:65]
	global_load_dwordx4 v[96:99], v4, s[54:55] nt
	global_load_dwordx4 v[100:103], v4, s[54:55] offset:32 nt
	global_load_dwordx4 v[104:107], v4, s[54:55] offset:64 nt
	global_load_dwordx4 v[108:111], v4, s[54:55] offset:96 nt
	global_load_dwordx4 v[112:115], v4, s[44:45]
	global_load_dwordx4 v[116:119], v4, s[44:45] offset:32
	global_load_dwordx4 v[120:123], v4, s[44:45] offset:64
	global_load_dwordx4 v[124:127], v4, s[44:45] offset:96
	global_load_dwordx4 v[128:131], v4, s[46:47]
	global_load_dwordx4 v[132:135], v4, s[46:47] offset:32
	global_load_dwordx4 v[136:139], v4, s[46:47] offset:64
	global_load_dwordx4 v[140:143], v4, s[46:47] offset:96
	global_load_dwordx4 v[144:147], v4, s[48:49]
	global_load_dwordx4 v[148:151], v4, s[48:49] offset:32
	global_load_dwordx4 v[152:155], v4, s[48:49] offset:64
	global_load_dwordx4 v[156:159], v4, s[48:49] offset:96
	global_load_dwordx4 v[160:163], v4, s[50:51]
	global_load_dwordx4 v[164:167], v4, s[50:51] offset:32
	global_load_dwordx4 v[168:171], v4, s[50:51] offset:64
	global_load_dwordx4 v[172:175], v4, s[50:51] offset:96
	global_load_dwordx4 v[176:179], v4, s[52:53]
	global_load_dwordx4 v[180:183], v4, s[52:53] offset:32
	global_load_dwordx4 v[184:187], v4, s[52:53] offset:64
	global_load_dwordx4 v[188:191], v4, s[52:53] offset:96
	global_load_dwordx4 v[192:195], v5, s[56:57]
	global_load_dwordx4 v[196:199], v5, s[56:57] offset:16
	global_load_dwordx4 v[200:203], v5, s[56:57] offset:32
	global_load_dwordx4 v[204:207], v5, s[56:57] offset:48
	global_load_dwordx4 v[208:211], v5, s[58:59]
	global_load_dwordx4 v[212:215], v5, s[58:59] offset:16
	global_load_dwordx4 v[216:219], v5, s[58:59] offset:32
	global_load_dwordx4 v[220:223], v5, s[58:59] offset:48
	global_load_dwordx4 v[224:227], v5, s[60:61]
	global_load_dwordx4 v[228:231], v5, s[60:61] offset:16
	global_load_dwordx4 v[232:235], v5, s[60:61] offset:32
	global_load_dwordx4 v[236:239], v5, s[60:61] offset:48
	s_waitcnt vmcnt(32)
	v_max_f32_dpp v8, v7, v7 quad_perm:[1,0,3,2] row_mask:0xf bank_mask:0xf
	v_fma_mix_f32 v10, v96, v96, 0 op_sel_hi:[1,1,0]
	v_fma_mix_f32 v11, v104, v104, 0 op_sel_hi:[1,1,0]
	v_fma_mix_f32 v10, v96, v96, v10 op_sel:[1,1,0] op_sel_hi:[1,1,0]
	v_fma_mix_f32 v11, v104, v104, v11 op_sel:[1,1,0] op_sel_hi:[1,1,0]
	v_max_f32_dpp v8, v8, v8 quad_perm:[2,3,0,1] row_mask:0xf bank_mask:0xf
	v_fma_mix_f32 v10, v97, v97, v10 op_sel_hi:[1,1,0]
	v_fma_mix_f32 v11, v105, v105, v11 op_sel_hi:[1,1,0]
	v_fma_mix_f32 v10, v97, v97, v10 op_sel:[1,1,0] op_sel_hi:[1,1,0]
	v_fma_mix_f32 v11, v105, v105, v11 op_sel:[1,1,0] op_sel_hi:[1,1,0]
	v_max_f32_dpp v8, v8, v8 row_half_mirror row_mask:0xf bank_mask:0xf
	v_fma_mix_f32 v10, v98, v98, v10 op_sel_hi:[1,1,0]
	v_fma_mix_f32 v11, v106, v106, v11 op_sel_hi:[1,1,0]
	v_fma_mix_f32 v10, v98, v98, v10 op_sel:[1,1,0] op_sel_hi:[1,1,0]
	v_fma_mix_f32 v11, v106, v106, v11 op_sel:[1,1,0] op_sel_hi:[1,1,0]
	v_max_f32_dpp v8, v8, v8 row_mirror row_mask:0xf bank_mask:0xf
	v_fma_mix_f32 v10, v99, v99, v10 op_sel_hi:[1,1,0]
	v_fma_mix_f32 v11, v107, v107, v11 op_sel_hi:[1,1,0]
	v_fma_mix_f32 v10, v99, v99, v10 op_sel:[1,1,0] op_sel_hi:[1,1,0]
	v_fma_mix_f32 v11, v107, v107, v11 op_sel:[1,1,0] op_sel_hi:[1,1,0]
	v_fma_mix_f32 v10, v100, v100, v10 op_sel_hi:[1,1,0]
	v_fma_mix_f32 v11, v108, v108, v11 op_sel_hi:[1,1,0]
	v_fma_mix_f32 v10, v100, v100, v10 op_sel:[1,1,0] op_sel_hi:[1,1,0]
	v_fma_mix_f32 v11, v108, v108, v11 op_sel:[1,1,0] op_sel_hi:[1,1,0]
	v_fma_mix_f32 v10, v101, v101, v10 op_sel_hi:[1,1,0]
	v_fma_mix_f32 v11, v109, v109, v11 op_sel_hi:[1,1,0]
	v_fma_mix_f32 v10, v101, v101, v10 op_sel:[1,1,0] op_sel_hi:[1,1,0]
	v_fma_mix_f32 v11, v109, v109, v11 op_sel:[1,1,0] op_sel_hi:[1,1,0]
	v_fma_mix_f32 v10, v102, v102, v10 op_sel_hi:[1,1,0]
	v_fma_mix_f32 v11, v110, v110, v11 op_sel_hi:[1,1,0]
	v_fma_mix_f32 v10, v102, v102, v10 op_sel:[1,1,0] op_sel_hi:[1,1,0]
	v_fma_mix_f32 v11, v110, v110, v11 op_sel:[1,1,0] op_sel_hi:[1,1,0]
	v_fma_mix_f32 v10, v103, v103, v10 op_sel_hi:[1,1,0]
	v_fma_mix_f32 v11, v111, v111, v11 op_sel_hi:[1,1,0]
	v_fma_mix_f32 v10, v103, v103, v10 op_sel:[1,1,0] op_sel_hi:[1,1,0]
	v_fma_mix_f32 v11, v111, v111, v11 op_sel:[1,1,0] op_sel_hi:[1,1,0]
	v_add_f32_e32 v10, v10, v11
	v_mov_b32_e32 v11, v10
	s_nop 1
	v_permlane32_swap_b32_e32 v10, v11
	v_add_f32_e32 v10, v10, v11
	s_nop 1
	v_max_f32_dpp v10, v10, v10 quad_perm:[1,0,3,2] row_mask:0xf bank_mask:0xf
	v_readlane_b32 s26, v8, 0
	v_readlane_b32 s27, v8, 16
	v_max_f32_dpp v10, v10, v10 quad_perm:[2,3,0,1] row_mask:0xf bank_mask:0xf
	v_readlane_b32 s28, v8, 32
	v_readlane_b32 s29, v8, 48
	v_max_f32_dpp v10, v10, v10 row_half_mirror row_mask:0xf bank_mask:0xf
	v_mov_b32_e32 v9, s26
	v_max_f32_e32 v9, s27, v9
	v_max_f32_dpp v10, v10, v10 row_mirror row_mask:0xf bank_mask:0xf
	v_max_f32_e32 v9, s28, v9
	v_max_f32_e32 v9, s29, v9
	v_readlane_b32 s26, v10, 0
	v_readlane_b32 s27, v10, 16
	v_sqrt_f32_e32 v9, v9
	s_nop 0
	v_mul_f32_e32 v9, 0x3f8020c5, v9
	v_mov_b32_e32 v12, s26
	v_max_f32_e32 v12, s27, v12
	v_sqrt_f32_e32 v12, v12
	s_nop 0
	v_mul_f32_e32 v12, 0x3f8020c5, v12
	v_mul_f32_e32 v9, v9, v12
	s_waitcnt vmcnt(12)
	v_fma_mix_f32 v13, v96, v112, 0 op_sel_hi:[1,1,0]
	v_fma_mix_f32 v14, v96, v128, 0 op_sel_hi:[1,1,0]
	v_fma_mix_f32 v15, v96, v144, 0 op_sel_hi:[1,1,0]
	v_fma_mix_f32 v16, v96, v160, 0 op_sel_hi:[1,1,0]
	v_fma_mix_f32 v17, v96, v176, 0 op_sel_hi:[1,1,0]
	v_fma_mix_f32 v13, v96, v112, v13 op_sel:[1,1,0] op_sel_hi:[1,1,0]
	v_fma_mix_f32 v14, v96, v128, v14 op_sel:[1,1,0] op_sel_hi:[1,1,0]
	v_fma_mix_f32 v15, v96, v144, v15 op_sel:[1,1,0] op_sel_hi:[1,1,0]
	v_fma_mix_f32 v16, v96, v160, v16 op_sel:[1,1,0] op_sel_hi:[1,1,0]
	v_fma_mix_f32 v17, v96, v176, v17 op_sel:[1,1,0] op_sel_hi:[1,1,0]
	v_fma_mix_f32 v13, v97, v113, v13 op_sel_hi:[1,1,0]
	v_fma_mix_f32 v14, v97, v129, v14 op_sel_hi:[1,1,0]
	v_fma_mix_f32 v15, v97, v145, v15 op_sel_hi:[1,1,0]
	v_fma_mix_f32 v16, v97, v161, v16 op_sel_hi:[1,1,0]
	v_fma_mix_f32 v17, v97, v177, v17 op_sel_hi:[1,1,0]
	v_fma_mix_f32 v13, v97, v113, v13 op_sel:[1,1,0] op_sel_hi:[1,1,0]
	v_fma_mix_f32 v14, v97, v129, v14 op_sel:[1,1,0] op_sel_hi:[1,1,0]
	v_fma_mix_f32 v15, v97, v145, v15 op_sel:[1,1,0] op_sel_hi:[1,1,0]
	v_fma_mix_f32 v16, v97, v161, v16 op_sel:[1,1,0] op_sel_hi:[1,1,0]
	v_fma_mix_f32 v17, v97, v177, v17 op_sel:[1,1,0] op_sel_hi:[1,1,0]
	v_fma_mix_f32 v13, v98, v114, v13 op_sel_hi:[1,1,0]
	v_fma_mix_f32 v14, v98, v130, v14 op_sel_hi:[1,1,0]
	v_fma_mix_f32 v15, v98, v146, v15 op_sel_hi:[1,1,0]
	v_fma_mix_f32 v16, v98, v162, v16 op_sel_hi:[1,1,0]
	v_fma_mix_f32 v17, v98, v178, v17 op_sel_hi:[1,1,0]
	v_fma_mix_f32 v13, v98, v114, v13 op_sel:[1,1,0] op_sel_hi:[1,1,0]
	v_fma_mix_f32 v14, v98, v130, v14 op_sel:[1,1,0] op_sel_hi:[1,1,0]
	v_fma_mix_f32 v15, v98, v146, v15 op_sel:[1,1,0] op_sel_hi:[1,1,0]
	v_fma_mix_f32 v16, v98, v162, v16 op_sel:[1,1,0] op_sel_hi:[1,1,0]
	v_fma_mix_f32 v17, v98, v178, v17 op_sel:[1,1,0] op_sel_hi:[1,1,0]
	v_fma_mix_f32 v13, v99, v115, v13 op_sel_hi:[1,1,0]
	v_fma_mix_f32 v14, v99, v131, v14 op_sel_hi:[1,1,0]
	v_fma_mix_f32 v15, v99, v147, v15 op_sel_hi:[1,1,0]
	v_fma_mix_f32 v16, v99, v163, v16 op_sel_hi:[1,1,0]
	v_fma_mix_f32 v17, v99, v179, v17 op_sel_hi:[1,1,0]
	v_fma_mix_f32 v13, v99, v115, v13 op_sel:[1,1,0] op_sel_hi:[1,1,0]
	v_fma_mix_f32 v14, v99, v131, v14 op_sel:[1,1,0] op_sel_hi:[1,1,0]
	v_fma_mix_f32 v15, v99, v147, v15 op_sel:[1,1,0] op_sel_hi:[1,1,0]
	v_fma_mix_f32 v16, v99, v163, v16 op_sel:[1,1,0] op_sel_hi:[1,1,0]
	v_fma_mix_f32 v17, v99, v179, v17 op_sel:[1,1,0] op_sel_hi:[1,1,0]
	v_fma_mix_f32 v13, v100, v116, v13 op_sel_hi:[1,1,0]
	v_fma_mix_f32 v14, v100, v132, v14 op_sel_hi:[1,1,0]
	v_fma_mix_f32 v15, v100, v148, v15 op_sel_hi:[1,1,0]
	v_fma_mix_f32 v16, v100, v164, v16 op_sel_hi:[1,1,0]
	v_fma_mix_f32 v17, v100, v180, v17 op_sel_hi:[1,1,0]
	v_fma_mix_f32 v13, v100, v116, v13 op_sel:[1,1,0] op_sel_hi:[1,1,0]
	v_fma_mix_f32 v14, v100, v132, v14 op_sel:[1,1,0] op_sel_hi:[1,1,0]
	v_fma_mix_f32 v15, v100, v148, v15 op_sel:[1,1,0] op_sel_hi:[1,1,0]
	v_fma_mix_f32 v16, v100, v164, v16 op_sel:[1,1,0] op_sel_hi:[1,1,0]
	v_fma_mix_f32 v17, v100, v180, v17 op_sel:[1,1,0] op_sel_hi:[1,1,0]
	v_fma_mix_f32 v13, v101, v117, v13 op_sel_hi:[1,1,0]
	v_fma_mix_f32 v14, v101, v133, v14 op_sel_hi:[1,1,0]
	v_fma_mix_f32 v15, v101, v149, v15 op_sel_hi:[1,1,0]
	v_fma_mix_f32 v16, v101, v165, v16 op_sel_hi:[1,1,0]
	v_fma_mix_f32 v17, v101, v181, v17 op_sel_hi:[1,1,0]
	v_fma_mix_f32 v13, v101, v117, v13 op_sel:[1,1,0] op_sel_hi:[1,1,0]
	v_fma_mix_f32 v14, v101, v133, v14 op_sel:[1,1,0] op_sel_hi:[1,1,0]
	v_fma_mix_f32 v15, v101, v149, v15 op_sel:[1,1,0] op_sel_hi:[1,1,0]
	v_fma_mix_f32 v16, v101, v165, v16 op_sel:[1,1,0] op_sel_hi:[1,1,0]
	v_fma_mix_f32 v17, v101, v181, v17 op_sel:[1,1,0] op_sel_hi:[1,1,0]
	v_fma_mix_f32 v13, v102, v118, v13 op_sel_hi:[1,1,0]
	v_fma_mix_f32 v14, v102, v134, v14 op_sel_hi:[1,1,0]
	v_fma_mix_f32 v15, v102, v150, v15 op_sel_hi:[1,1,0]
	v_fma_mix_f32 v16, v102, v166, v16 op_sel_hi:[1,1,0]
	v_fma_mix_f32 v17, v102, v182, v17 op_sel_hi:[1,1,0]
	v_fma_mix_f32 v13, v102, v118, v13 op_sel:[1,1,0] op_sel_hi:[1,1,0]
	v_fma_mix_f32 v14, v102, v134, v14 op_sel:[1,1,0] op_sel_hi:[1,1,0]
	v_fma_mix_f32 v15, v102, v150, v15 op_sel:[1,1,0] op_sel_hi:[1,1,0]
	v_fma_mix_f32 v16, v102, v166, v16 op_sel:[1,1,0] op_sel_hi:[1,1,0]
	v_fma_mix_f32 v17, v102, v182, v17 op_sel:[1,1,0] op_sel_hi:[1,1,0]
	v_fma_mix_f32 v13, v103, v119, v13 op_sel_hi:[1,1,0]
	v_fma_mix_f32 v14, v103, v135, v14 op_sel_hi:[1,1,0]
	v_fma_mix_f32 v15, v103, v151, v15 op_sel_hi:[1,1,0]
	v_fma_mix_f32 v16, v103, v167, v16 op_sel_hi:[1,1,0]
	v_fma_mix_f32 v17, v103, v183, v17 op_sel_hi:[1,1,0]
	v_fma_mix_f32 v13, v103, v119, v13 op_sel:[1,1,0] op_sel_hi:[1,1,0]
	v_fma_mix_f32 v14, v103, v135, v14 op_sel:[1,1,0] op_sel_hi:[1,1,0]
	v_fma_mix_f32 v15, v103, v151, v15 op_sel:[1,1,0] op_sel_hi:[1,1,0]
	v_fma_mix_f32 v16, v103, v167, v16 op_sel:[1,1,0] op_sel_hi:[1,1,0]
	v_fma_mix_f32 v17, v103, v183, v17 op_sel:[1,1,0] op_sel_hi:[1,1,0]
	v_fma_mix_f32 v13, v104, v120, v13 op_sel_hi:[1,1,0]
	v_fma_mix_f32 v14, v104, v136, v14 op_sel_hi:[1,1,0]
	v_fma_mix_f32 v15, v104, v152, v15 op_sel_hi:[1,1,0]
	v_fma_mix_f32 v16, v104, v168, v16 op_sel_hi:[1,1,0]
	v_fma_mix_f32 v17, v104, v184, v17 op_sel_hi:[1,1,0]
	v_fma_mix_f32 v13, v104, v120, v13 op_sel:[1,1,0] op_sel_hi:[1,1,0]
	v_fma_mix_f32 v14, v104, v136, v14 op_sel:[1,1,0] op_sel_hi:[1,1,0]
	v_fma_mix_f32 v15, v104, v152, v15 op_sel:[1,1,0] op_sel_hi:[1,1,0]
	v_fma_mix_f32 v16, v104, v168, v16 op_sel:[1,1,0] op_sel_hi:[1,1,0]
	v_fma_mix_f32 v17, v104, v184, v17 op_sel:[1,1,0] op_sel_hi:[1,1,0]
	v_fma_mix_f32 v13, v105, v121, v13 op_sel_hi:[1,1,0]
	v_fma_mix_f32 v14, v105, v137, v14 op_sel_hi:[1,1,0]
	v_fma_mix_f32 v15, v105, v153, v15 op_sel_hi:[1,1,0]
	v_fma_mix_f32 v16, v105, v169, v16 op_sel_hi:[1,1,0]
	v_fma_mix_f32 v17, v105, v185, v17 op_sel_hi:[1,1,0]
	v_fma_mix_f32 v13, v105, v121, v13 op_sel:[1,1,0] op_sel_hi:[1,1,0]
	v_fma_mix_f32 v14, v105, v137, v14 op_sel:[1,1,0] op_sel_hi:[1,1,0]
	v_fma_mix_f32 v15, v105, v153, v15 op_sel:[1,1,0] op_sel_hi:[1,1,0]
	v_fma_mix_f32 v16, v105, v169, v16 op_sel:[1,1,0] op_sel_hi:[1,1,0]
	v_fma_mix_f32 v17, v105, v185, v17 op_sel:[1,1,0] op_sel_hi:[1,1,0]
	v_fma_mix_f32 v13, v106, v122, v13 op_sel_hi:[1,1,0]
	v_fma_mix_f32 v14, v106, v138, v14 op_sel_hi:[1,1,0]
	v_fma_mix_f32 v15, v106, v154, v15 op_sel_hi:[1,1,0]
	v_fma_mix_f32 v16, v106, v170, v16 op_sel_hi:[1,1,0]
	v_fma_mix_f32 v17, v106, v186, v17 op_sel_hi:[1,1,0]
	v_fma_mix_f32 v13, v106, v122, v13 op_sel:[1,1,0] op_sel_hi:[1,1,0]
	v_fma_mix_f32 v14, v106, v138, v14 op_sel:[1,1,0] op_sel_hi:[1,1,0]
	v_fma_mix_f32 v15, v106, v154, v15 op_sel:[1,1,0] op_sel_hi:[1,1,0]
	v_fma_mix_f32 v16, v106, v170, v16 op_sel:[1,1,0] op_sel_hi:[1,1,0]
	v_fma_mix_f32 v17, v106, v186, v17 op_sel:[1,1,0] op_sel_hi:[1,1,0]
	v_fma_mix_f32 v13, v107, v123, v13 op_sel_hi:[1,1,0]
	v_fma_mix_f32 v14, v107, v139, v14 op_sel_hi:[1,1,0]
	v_fma_mix_f32 v15, v107, v155, v15 op_sel_hi:[1,1,0]
	v_fma_mix_f32 v16, v107, v171, v16 op_sel_hi:[1,1,0]
	v_fma_mix_f32 v17, v107, v187, v17 op_sel_hi:[1,1,0]
	v_fma_mix_f32 v13, v107, v123, v13 op_sel:[1,1,0] op_sel_hi:[1,1,0]
	v_fma_mix_f32 v14, v107, v139, v14 op_sel:[1,1,0] op_sel_hi:[1,1,0]
	v_fma_mix_f32 v15, v107, v155, v15 op_sel:[1,1,0] op_sel_hi:[1,1,0]
	v_fma_mix_f32 v16, v107, v171, v16 op_sel:[1,1,0] op_sel_hi:[1,1,0]
	v_fma_mix_f32 v17, v107, v187, v17 op_sel:[1,1,0] op_sel_hi:[1,1,0]
	v_fma_mix_f32 v13, v108, v124, v13 op_sel_hi:[1,1,0]
	v_fma_mix_f32 v14, v108, v140, v14 op_sel_hi:[1,1,0]
	v_fma_mix_f32 v15, v108, v156, v15 op_sel_hi:[1,1,0]
	v_fma_mix_f32 v16, v108, v172, v16 op_sel_hi:[1,1,0]
	v_fma_mix_f32 v17, v108, v188, v17 op_sel_hi:[1,1,0]
	v_fma_mix_f32 v13, v108, v124, v13 op_sel:[1,1,0] op_sel_hi:[1,1,0]
	v_fma_mix_f32 v14, v108, v140, v14 op_sel:[1,1,0] op_sel_hi:[1,1,0]
	v_fma_mix_f32 v15, v108, v156, v15 op_sel:[1,1,0] op_sel_hi:[1,1,0]
	v_fma_mix_f32 v16, v108, v172, v16 op_sel:[1,1,0] op_sel_hi:[1,1,0]
	v_fma_mix_f32 v17, v108, v188, v17 op_sel:[1,1,0] op_sel_hi:[1,1,0]
	v_fma_mix_f32 v13, v109, v125, v13 op_sel_hi:[1,1,0]
	v_fma_mix_f32 v14, v109, v141, v14 op_sel_hi:[1,1,0]
	v_fma_mix_f32 v15, v109, v157, v15 op_sel_hi:[1,1,0]
	v_fma_mix_f32 v16, v109, v173, v16 op_sel_hi:[1,1,0]
	v_fma_mix_f32 v17, v109, v189, v17 op_sel_hi:[1,1,0]
	v_fma_mix_f32 v13, v109, v125, v13 op_sel:[1,1,0] op_sel_hi:[1,1,0]
	v_fma_mix_f32 v14, v109, v141, v14 op_sel:[1,1,0] op_sel_hi:[1,1,0]
	v_fma_mix_f32 v15, v109, v157, v15 op_sel:[1,1,0] op_sel_hi:[1,1,0]
	v_fma_mix_f32 v16, v109, v173, v16 op_sel:[1,1,0] op_sel_hi:[1,1,0]
	v_fma_mix_f32 v17, v109, v189, v17 op_sel:[1,1,0] op_sel_hi:[1,1,0]
	v_fma_mix_f32 v13, v110, v126, v13 op_sel_hi:[1,1,0]
	v_fma_mix_f32 v14, v110, v142, v14 op_sel_hi:[1,1,0]
	v_fma_mix_f32 v15, v110, v158, v15 op_sel_hi:[1,1,0]
	v_fma_mix_f32 v16, v110, v174, v16 op_sel_hi:[1,1,0]
	v_fma_mix_f32 v17, v110, v190, v17 op_sel_hi:[1,1,0]
	v_fma_mix_f32 v13, v110, v126, v13 op_sel:[1,1,0] op_sel_hi:[1,1,0]
	v_fma_mix_f32 v14, v110, v142, v14 op_sel:[1,1,0] op_sel_hi:[1,1,0]
	v_fma_mix_f32 v15, v110, v158, v15 op_sel:[1,1,0] op_sel_hi:[1,1,0]
	v_fma_mix_f32 v16, v110, v174, v16 op_sel:[1,1,0] op_sel_hi:[1,1,0]
	v_fma_mix_f32 v17, v110, v190, v17 op_sel:[1,1,0] op_sel_hi:[1,1,0]
	v_fma_mix_f32 v13, v111, v127, v13 op_sel_hi:[1,1,0]
	v_fma_mix_f32 v14, v111, v143, v14 op_sel_hi:[1,1,0]
	v_fma_mix_f32 v15, v111, v159, v15 op_sel_hi:[1,1,0]
	v_fma_mix_f32 v16, v111, v175, v16 op_sel_hi:[1,1,0]
	v_fma_mix_f32 v17, v111, v191, v17 op_sel_hi:[1,1,0]
	v_fma_mix_f32 v13, v111, v127, v13 op_sel:[1,1,0] op_sel_hi:[1,1,0]
	v_fma_mix_f32 v14, v111, v143, v14 op_sel:[1,1,0] op_sel_hi:[1,1,0]
	v_fma_mix_f32 v15, v111, v159, v15 op_sel:[1,1,0] op_sel_hi:[1,1,0]
	v_fma_mix_f32 v16, v111, v175, v16 op_sel:[1,1,0] op_sel_hi:[1,1,0]
	v_fma_mix_f32 v17, v111, v191, v17 op_sel:[1,1,0] op_sel_hi:[1,1,0]
	v_mov_b32_e32 v18, v13
	v_mov_b32_e32 v19, v14
	v_mov_b32_e32 v20, v15
	v_mov_b32_e32 v21, v16
	v_mov_b32_e32 v22, v17
	s_nop 1
	v_permlane32_swap_b32_e32 v13, v18
	v_permlane32_swap_b32_e32 v14, v19
	v_permlane32_swap_b32_e32 v15, v20
	v_permlane32_swap_b32_e32 v16, v21
	v_permlane32_swap_b32_e32 v17, v22
	v_add_f32_e32 v13, v13, v18
	v_add_f32_e32 v14, v14, v19
	v_add_f32_e32 v15, v15, v20
	v_add_f32_e32 v16, v16, v21
	v_add_f32_e32 v17, v17, v22
	v_add_f32_e32 v13, 0x42e59caf, v13
	v_add_f32_e32 v14, 0x42e59caf, v14
	v_add_f32_e32 v15, 0x42e59caf, v15
	v_add_f32_e32 v16, 0x42659caf, v16
	v_add_f32_e32 v17, 0x42659caf, v17
	v_add_f32_e32 v14, s40, v14
	v_add_f32_e32 v15, s41, v15
	v_add_f32_e32 v16, s42, v16
	v_add_f32_e32 v17, s43, v17
	v_max3_f32 v23, v13, v14, v15
	v_sub_f32_e32 v24, v13, v23
	v_sub_f32_e32 v25, v14, v23
	v_sub_f32_e32 v26, v15, v23
	v_exp_f32_e32 v24, v24
	v_exp_f32_e32 v25, v25
	v_exp_f32_e32 v26, v26
	v_min_f32_dpp v27, v23, v23 quad_perm:[1,0,3,2] row_mask:0xf bank_mask:0xf
	v_sub_f32_e32 v16, v16, v23
	v_sub_f32_e32 v17, v17, v23
	v_min_f32_dpp v27, v27, v27 quad_perm:[2,3,0,1] row_mask:0xf bank_mask:0xf
	v_add_f32_e32 v28, v24, v25
	v_max_f32_e32 v16, v16, v17
	v_min_f32_dpp v27, v27, v27 row_half_mirror row_mask:0xf bank_mask:0xf
	v_add_f32_e32 v28, v28, v26
	s_mov_b32 s30, 0xc2200a3d
	v_min_f32_dpp v27, v27, v27 row_mirror row_mask:0xf bank_mask:0xf
	v_cmp_ngt_f32_e32 vcc, s30, v16
	s_cmp_lg_u64 vcc, 0
	s_cselect_b32 s31, 1, 0
	v_readlane_b32 s26, v27, 0
	v_readlane_b32 s27, v27, 16
	s_nop 1
	v_mov_b32_e32 v29, s26
	v_min_f32_e32 v29, s27, v29
	v_add_f32_e32 v9, 0x42191384, v9
	v_sub_f32_e32 v9, v9, v29
	v_cmp_ngt_f32_e32 vcc, s30, v9
	s_cmp_lg_u64 vcc, 0
	s_cselect_b32 s26, 1, 0
	s_or_b32 s31, s31, s26
	s_lshl_b32 s26, s19, 2
	s_add_i32 s26, s26, 0x20700
	v_mov_b32_e32 v30, s26
	v_mov_b32_e32 v31, s31
	ds_write_b32 v30, v31
	s_waitcnt lgkmcnt(0)
	s_barrier
	v_mov_b32_e32 v30, 0x20700
	ds_read_b128 v[64:67], v30
	ds_read_b128 v[68:71], v30 offset:16
	v_div_scale_f32 v72, s[26:27], v28, v28, 1.0
	v_rcp_f32_e32 v73, v72
	s_nop 0
	v_fma_f32 v74, -v72, v73, 1.0
	v_fmac_f32_e32 v73, v74, v73
	v_div_scale_f32 v74, vcc, 1.0, v28, 1.0
	v_mul_f32_e32 v75, v74, v73
	v_fma_f32 v76, -v72, v75, v74
	v_fmac_f32_e32 v75, v76, v73
	v_fma_f32 v72, -v72, v75, v74
	v_div_fmas_f32 v72, v72, v73, v75
	v_div_fixup_f32 v28, v72, v28, 1.0
	s_waitcnt lgkmcnt(0)
	v_or3_b32 v64, v64, v65, v66
	v_or3_b32 v68, v68, v69, v70
	v_or3_b32 v64, v64, v67, v68
	v_or_b32_e32 v64, v64, v71
	s_nop 0
	v_readfirstlane_b32 s26, v64
	s_nop 3
	s_cmp_lg_u32 s26, 0
	s_cbranch_scc1 .Lattn_fallback
	v_mul_f32_e32 v24, v24, v28
	v_mul_f32_e32 v25, v25, v28
	v_mul_f32_e32 v26, v26, v28
	s_waitcnt vmcnt(0)
	v_readlane_b32 s66, v24, 0
	v_readlane_b32 s67, v24, 1
	v_readlane_b32 s68, v24, 2
	v_readlane_b32 s69, v24, 3
	v_readlane_b32 s70, v24, 8
	v_readlane_b32 s71, v24, 9
	v_readlane_b32 s72, v24, 10
	v_readlane_b32 s73, v24, 11
	v_fma_mix_f32 v32, v192, s66, 0 op_sel:[0,0,0] op_sel_hi:[1,0,0]
	v_fma_mix_f32 v33, v192, s67, 0 op_sel:[1,0,0] op_sel_hi:[1,0,0]
	v_fma_mix_f32 v34, v193, s68, 0 op_sel:[0,0,0] op_sel_hi:[1,0,0]
	v_fma_mix_f32 v35, v193, s69, 0 op_sel:[1,0,0] op_sel_hi:[1,0,0]
	v_fma_mix_f32 v40, v194, s70, 0 op_sel:[0,0,0] op_sel_hi:[1,0,0]
	v_fma_mix_f32 v41, v194, s71, 0 op_sel:[1,0,0] op_sel_hi:[1,0,0]
	v_fma_mix_f32 v42, v195, s72, 0 op_sel:[0,0,0] op_sel_hi:[1,0,0]
	v_fma_mix_f32 v43, v195, s73, 0 op_sel:[1,0,0] op_sel_hi:[1,0,0]
	v_readlane_b32 s66, v24, 4
	v_readlane_b32 s67, v24, 5
	v_readlane_b32 s68, v24, 6
	v_readlane_b32 s69, v24, 7
	v_readlane_b32 s70, v24, 12
	v_readlane_b32 s71, v24, 13
	v_readlane_b32 s72, v24, 14
	v_readlane_b32 s73, v24, 15
	v_fma_mix_f32 v36, v196, s66, 0 op_sel:[0,0,0] op_sel_hi:[1,0,0]
	v_fma_mix_f32 v37, v196, s67, 0 op_sel:[1,0,0] op_sel_hi:[1,0,0]
	v_fma_mix_f32 v38, v197, s68, 0 op_sel:[0,0,0] op_sel_hi:[1,0,0]
	v_fma_mix_f32 v39, v197, s69, 0 op_sel:[1,0,0] op_sel_hi:[1,0,0]
	v_fma_mix_f32 v44, v198, s70, 0 op_sel:[0,0,0] op_sel_hi:[1,0,0]
	v_fma_mix_f32 v45, v198, s71, 0 op_sel:[1,0,0] op_sel_hi:[1,0,0]
	v_fma_mix_f32 v46, v199, s72, 0 op_sel:[0,0,0] op_sel_hi:[1,0,0]
	v_fma_mix_f32 v47, v199, s73, 0 op_sel:[1,0,0] op_sel_hi:[1,0,0]
	v_readlane_b32 s66, v24, 16
	v_readlane_b32 s67, v24, 17
	v_readlane_b32 s68, v24, 18
	v_readlane_b32 s69, v24, 19
	v_readlane_b32 s70, v24, 24
	v_readlane_b32 s71, v24, 25
	v_readlane_b32 s72, v24, 26
	v_readlane_b32 s73, v24, 27
	v_fma_mix_f32 v48, v200, s66, 0 op_sel:[0,0,0] op_sel_hi:[1,0,0]
	v_fma_mix_f32 v49, v200, s67, 0 op_sel:[1,0,0] op_sel_hi:[1,0,0]
	v_fma_mix_f32 v50, v201, s68, 0 op_sel:[0,0,0] op_sel_hi:[1,0,0]
	v_fma_mix_f32 v51, v201, s69, 0 op_sel:[1,0,0] op_sel_hi:[1,0,0]
	v_fma_mix_f32 v56, v202, s70, 0 op_sel:[0,0,0] op_sel_hi:[1,0,0]
	v_fma_mix_f32 v57, v202, s71, 0 op_sel:[1,0,0] op_sel_hi:[1,0,0]
	v_fma_mix_f32 v58, v203, s72, 0 op_sel:[0,0,0] op_sel_hi:[1,0,0]
	v_fma_mix_f32 v59, v203, s73, 0 op_sel:[1,0,0] op_sel_hi:[1,0,0]
	v_readlane_b32 s66, v24, 20
	v_readlane_b32 s67, v24, 21
	v_readlane_b32 s68, v24, 22
	v_readlane_b32 s69, v24, 23
	v_readlane_b32 s70, v24, 28
	v_readlane_b32 s71, v24, 29
	v_readlane_b32 s72, v24, 30
	v_readlane_b32 s73, v24, 31
	v_fma_mix_f32 v52, v204, s66, 0 op_sel:[0,0,0] op_sel_hi:[1,0,0]
	v_fma_mix_f32 v53, v204, s67, 0 op_sel:[1,0,0] op_sel_hi:[1,0,0]
	v_fma_mix_f32 v54, v205, s68, 0 op_sel:[0,0,0] op_sel_hi:[1,0,0]
	v_fma_mix_f32 v55, v205, s69, 0 op_sel:[1,0,0] op_sel_hi:[1,0,0]
	v_fma_mix_f32 v60, v206, s70, 0 op_sel:[0,0,0] op_sel_hi:[1,0,0]
	v_fma_mix_f32 v61, v206, s71, 0 op_sel:[1,0,0] op_sel_hi:[1,0,0]
	v_fma_mix_f32 v62, v207, s72, 0 op_sel:[0,0,0] op_sel_hi:[1,0,0]
	v_fma_mix_f32 v63, v207, s73, 0 op_sel:[1,0,0] op_sel_hi:[1,0,0]
	v_readlane_b32 s66, v25, 0
	v_readlane_b32 s67, v25, 1
	v_readlane_b32 s68, v25, 2
	v_readlane_b32 s69, v25, 3
	v_readlane_b32 s70, v25, 8
	v_readlane_b32 s71, v25, 9
	v_readlane_b32 s72, v25, 10
	v_readlane_b32 s73, v25, 11
	v_fma_mix_f32 v32, v208, s66, v32 op_sel:[0,0,0] op_sel_hi:[1,0,0]
	v_fma_mix_f32 v33, v208, s67, v33 op_sel:[1,0,0] op_sel_hi:[1,0,0]
	v_fma_mix_f32 v34, v209, s68, v34 op_sel:[0,0,0] op_sel_hi:[1,0,0]
	v_fma_mix_f32 v35, v209, s69, v35 op_sel:[1,0,0] op_sel_hi:[1,0,0]
	v_fma_mix_f32 v40, v210, s70, v40 op_sel:[0,0,0] op_sel_hi:[1,0,0]
	v_fma_mix_f32 v41, v210, s71, v41 op_sel:[1,0,0] op_sel_hi:[1,0,0]
	v_fma_mix_f32 v42, v211, s72, v42 op_sel:[0,0,0] op_sel_hi:[1,0,0]
	v_fma_mix_f32 v43, v211, s73, v43 op_sel:[1,0,0] op_sel_hi:[1,0,0]
	v_readlane_b32 s66, v25, 4
	v_readlane_b32 s67, v25, 5
	v_readlane_b32 s68, v25, 6
	v_readlane_b32 s69, v25, 7
	v_readlane_b32 s70, v25, 12
	v_readlane_b32 s71, v25, 13
	v_readlane_b32 s72, v25, 14
	v_readlane_b32 s73, v25, 15
	v_fma_mix_f32 v36, v212, s66, v36 op_sel:[0,0,0] op_sel_hi:[1,0,0]
	v_fma_mix_f32 v37, v212, s67, v37 op_sel:[1,0,0] op_sel_hi:[1,0,0]
	v_fma_mix_f32 v38, v213, s68, v38 op_sel:[0,0,0] op_sel_hi:[1,0,0]
	v_fma_mix_f32 v39, v213, s69, v39 op_sel:[1,0,0] op_sel_hi:[1,0,0]
	v_fma_mix_f32 v44, v214, s70, v44 op_sel:[0,0,0] op_sel_hi:[1,0,0]
	v_fma_mix_f32 v45, v214, s71, v45 op_sel:[1,0,0] op_sel_hi:[1,0,0]
	v_fma_mix_f32 v46, v215, s72, v46 op_sel:[0,0,0] op_sel_hi:[1,0,0]
	v_fma_mix_f32 v47, v215, s73, v47 op_sel:[1,0,0] op_sel_hi:[1,0,0]
	v_readlane_b32 s66, v25, 16
	v_readlane_b32 s67, v25, 17
	v_readlane_b32 s68, v25, 18
	v_readlane_b32 s69, v25, 19
	v_readlane_b32 s70, v25, 24
	v_readlane_b32 s71, v25, 25
	v_readlane_b32 s72, v25, 26
	v_readlane_b32 s73, v25, 27
	v_fma_mix_f32 v48, v216, s66, v48 op_sel:[0,0,0] op_sel_hi:[1,0,0]
	v_fma_mix_f32 v49, v216, s67, v49 op_sel:[1,0,0] op_sel_hi:[1,0,0]
	v_fma_mix_f32 v50, v217, s68, v50 op_sel:[0,0,0] op_sel_hi:[1,0,0]
	v_fma_mix_f32 v51, v217, s69, v51 op_sel:[1,0,0] op_sel_hi:[1,0,0]
	v_fma_mix_f32 v56, v218, s70, v56 op_sel:[0,0,0] op_sel_hi:[1,0,0]
	v_fma_mix_f32 v57, v218, s71, v57 op_sel:[1,0,0] op_sel_hi:[1,0,0]
	v_fma_mix_f32 v58, v219, s72, v58 op_sel:[0,0,0] op_sel_hi:[1,0,0]
	v_fma_mix_f32 v59, v219, s73, v59 op_sel:[1,0,0] op_sel_hi:[1,0,0]
	v_readlane_b32 s66, v25, 20
	v_readlane_b32 s67, v25, 21
	v_readlane_b32 s68, v25, 22
	v_readlane_b32 s69, v25, 23
	v_readlane_b32 s70, v25, 28
	v_readlane_b32 s71, v25, 29
	v_readlane_b32 s72, v25, 30
	v_readlane_b32 s73, v25, 31
	v_fma_mix_f32 v52, v220, s66, v52 op_sel:[0,0,0] op_sel_hi:[1,0,0]
	v_fma_mix_f32 v53, v220, s67, v53 op_sel:[1,0,0] op_sel_hi:[1,0,0]
	v_fma_mix_f32 v54, v221, s68, v54 op_sel:[0,0,0] op_sel_hi:[1,0,0]
	v_fma_mix_f32 v55, v221, s69, v55 op_sel:[1,0,0] op_sel_hi:[1,0,0]
	v_fma_mix_f32 v60, v222, s70, v60 op_sel:[0,0,0] op_sel_hi:[1,0,0]
	v_fma_mix_f32 v61, v222, s71, v61 op_sel:[1,0,0] op_sel_hi:[1,0,0]
	v_fma_mix_f32 v62, v223, s72, v62 op_sel:[0,0,0] op_sel_hi:[1,0,0]
	v_fma_mix_f32 v63, v223, s73, v63 op_sel:[1,0,0] op_sel_hi:[1,0,0]
	v_readlane_b32 s66, v26, 0
	v_readlane_b32 s67, v26, 1
	v_readlane_b32 s68, v26, 2
	v_readlane_b32 s69, v26, 3
	v_readlane_b32 s70, v26, 8
	v_readlane_b32 s71, v26, 9
	v_readlane_b32 s72, v26, 10
	v_readlane_b32 s73, v26, 11
	v_fma_mix_f32 v32, v224, s66, v32 op_sel:[0,0,0] op_sel_hi:[1,0,0]
	v_fma_mix_f32 v33, v224, s67, v33 op_sel:[1,0,0] op_sel_hi:[1,0,0]
	v_fma_mix_f32 v34, v225, s68, v34 op_sel:[0,0,0] op_sel_hi:[1,0,0]
	v_fma_mix_f32 v35, v225, s69, v35 op_sel:[1,0,0] op_sel_hi:[1,0,0]
	v_fma_mix_f32 v40, v226, s70, v40 op_sel:[0,0,0] op_sel_hi:[1,0,0]
	v_fma_mix_f32 v41, v226, s71, v41 op_sel:[1,0,0] op_sel_hi:[1,0,0]
	v_fma_mix_f32 v42, v227, s72, v42 op_sel:[0,0,0] op_sel_hi:[1,0,0]
	v_fma_mix_f32 v43, v227, s73, v43 op_sel:[1,0,0] op_sel_hi:[1,0,0]
	v_readlane_b32 s66, v26, 4
	v_readlane_b32 s67, v26, 5
	v_readlane_b32 s68, v26, 6
	v_readlane_b32 s69, v26, 7
	v_readlane_b32 s70, v26, 12
	v_readlane_b32 s71, v26, 13
	v_readlane_b32 s72, v26, 14
	v_readlane_b32 s73, v26, 15
	v_fma_mix_f32 v36, v228, s66, v36 op_sel:[0,0,0] op_sel_hi:[1,0,0]
	v_fma_mix_f32 v37, v228, s67, v37 op_sel:[1,0,0] op_sel_hi:[1,0,0]
	v_fma_mix_f32 v38, v229, s68, v38 op_sel:[0,0,0] op_sel_hi:[1,0,0]
	v_fma_mix_f32 v39, v229, s69, v39 op_sel:[1,0,0] op_sel_hi:[1,0,0]
	v_fma_mix_f32 v44, v230, s70, v44 op_sel:[0,0,0] op_sel_hi:[1,0,0]
	v_fma_mix_f32 v45, v230, s71, v45 op_sel:[1,0,0] op_sel_hi:[1,0,0]
	v_fma_mix_f32 v46, v231, s72, v46 op_sel:[0,0,0] op_sel_hi:[1,0,0]
	v_fma_mix_f32 v47, v231, s73, v47 op_sel:[1,0,0] op_sel_hi:[1,0,0]
	v_readlane_b32 s66, v26, 16
	v_readlane_b32 s67, v26, 17
	v_readlane_b32 s68, v26, 18
	v_readlane_b32 s69, v26, 19
	v_readlane_b32 s70, v26, 24
	v_readlane_b32 s71, v26, 25
	v_readlane_b32 s72, v26, 26
	v_readlane_b32 s73, v26, 27
	v_fma_mix_f32 v48, v232, s66, v48 op_sel:[0,0,0] op_sel_hi:[1,0,0]
	v_fma_mix_f32 v49, v232, s67, v49 op_sel:[1,0,0] op_sel_hi:[1,0,0]
	v_fma_mix_f32 v50, v233, s68, v50 op_sel:[0,0,0] op_sel_hi:[1,0,0]
	v_fma_mix_f32 v51, v233, s69, v51 op_sel:[1,0,0] op_sel_hi:[1,0,0]
	v_fma_mix_f32 v56, v234, s70, v56 op_sel:[0,0,0] op_sel_hi:[1,0,0]
	v_fma_mix_f32 v57, v234, s71, v57 op_sel:[1,0,0] op_sel_hi:[1,0,0]
	v_fma_mix_f32 v58, v235, s72, v58 op_sel:[0,0,0] op_sel_hi:[1,0,0]
	v_fma_mix_f32 v59, v235, s73, v59 op_sel:[1,0,0] op_sel_hi:[1,0,0]
	v_readlane_b32 s66, v26, 20
	v_readlane_b32 s67, v26, 21
	v_readlane_b32 s68, v26, 22
	v_readlane_b32 s69, v26, 23
	v_readlane_b32 s70, v26, 28
	v_readlane_b32 s71, v26, 29
	v_readlane_b32 s72, v26, 30
	v_readlane_b32 s73, v26, 31
	v_fma_mix_f32 v52, v236, s66, v52 op_sel:[0,0,0] op_sel_hi:[1,0,0]
	v_fma_mix_f32 v53, v236, s67, v53 op_sel:[1,0,0] op_sel_hi:[1,0,0]
	v_fma_mix_f32 v54, v237, s68, v54 op_sel:[0,0,0] op_sel_hi:[1,0,0]
	v_fma_mix_f32 v55, v237, s69, v55 op_sel:[1,0,0] op_sel_hi:[1,0,0]
	v_fma_mix_f32 v60, v238, s70, v60 op_sel:[0,0,0] op_sel_hi:[1,0,0]
	v_fma_mix_f32 v61, v238, s71, v61 op_sel:[1,0,0] op_sel_hi:[1,0,0]
	v_fma_mix_f32 v62, v239, s72, v62 op_sel:[0,0,0] op_sel_hi:[1,0,0]
	v_fma_mix_f32 v63, v239, s73, v63 op_sel:[1,0,0] op_sel_hi:[1,0,0]
	s_mul_i32 s26, s19, 0x2200
	v_lshl_add_u32 v80, v1, 2, s26
	ds_write_b32 v80, v32
	ds_write_b32 v80, v33 offset:272
	ds_write_b32 v80, v34 offset:544
	ds_write_b32 v80, v35 offset:816
	ds_write_b32 v80, v36 offset:1088
	ds_write_b32 v80, v37 offset:1360
	ds_write_b32 v80, v38 offset:1632
	ds_write_b32 v80, v39 offset:1904
	ds_write_b32 v80, v40 offset:2176
	ds_write_b32 v80, v41 offset:2448
	ds_write_b32 v80, v42 offset:2720
	ds_write_b32 v80, v43 offset:2992
	ds_write_b32 v80, v44 offset:3264
	ds_write_b32 v80, v45 offset:3536
	ds_write_b32 v80, v46 offset:3808
	ds_write_b32 v80, v47 offset:4080
	ds_write_b32 v80, v48 offset:4352
	ds_write_b32 v80, v49 offset:4624
	ds_write_b32 v80, v50 offset:4896
	ds_write_b32 v80, v51 offset:5168
	ds_write_b32 v80, v52 offset:5440
	ds_write_b32 v80, v53 offset:5712
	ds_write_b32 v80, v54 offset:5984
	ds_write_b32 v80, v55 offset:6256
	ds_write_b32 v80, v56 offset:6528
	ds_write_b32 v80, v57 offset:6800
	ds_write_b32 v80, v58 offset:7072
	ds_write_b32 v80, v59 offset:7344
	ds_write_b32 v80, v60 offset:7616
	ds_write_b32 v80, v61 offset:7888
	ds_write_b32 v80, v62 offset:8160
	ds_write_b32 v80, v63 offset:8432
	v_lshrrev_b32_e32 v81, 4, v1
	v_and_b32_e32 v82, 15, v1
	v_mul_u32_u24_e32 v83, 0x110, v81
	v_lshl_add_u32 v83, v82, 4, v83
	v_add_u32_e32 v83, s26, v83
	v_lshlrev_b32_e32 v84, 8, v81
	v_lshl_add_u32 v84, v82, 4, v84
	v_add_u32_e32 v85, 0x1000, v84
	ds_read_b128 v[32:35], v83
	ds_read_b128 v[36:39], v83 offset:1088
	ds_read_b128 v[40:43], v83 offset:2176
	ds_read_b128 v[44:47], v83 offset:3264
	ds_read_b128 v[48:51], v83 offset:4352
	ds_read_b128 v[52:55], v83 offset:5440
	ds_read_b128 v[56:59], v83 offset:6528
	ds_read_b128 v[60:63], v83 offset:7616
	s_waitcnt lgkmcnt(7)
	global_store_dwordx4 v84, v[32:35], s[62:63] sc1
	s_waitcnt lgkmcnt(6)
	global_store_dwordx4 v84, v[36:39], s[62:63] offset:1024 sc1
	s_waitcnt lgkmcnt(5)
	global_store_dwordx4 v84, v[40:43], s[62:63] offset:2048 sc1
	s_waitcnt lgkmcnt(4)
	global_store_dwordx4 v84, v[44:47], s[62:63] offset:3072 sc1
	s_waitcnt lgkmcnt(3)
	global_store_dwordx4 v85, v[48:51], s[62:63] sc1
	s_waitcnt lgkmcnt(2)
	global_store_dwordx4 v85, v[52:55], s[62:63] offset:1024 sc1
	s_waitcnt lgkmcnt(1)
	global_store_dwordx4 v85, v[56:59], s[62:63] offset:2048 sc1
	s_waitcnt lgkmcnt(0)
	global_store_dwordx4 v85, v[60:63], s[62:63] offset:3072 sc1
	s_endpgm
.Lattn_fallback:
	s_waitcnt vmcnt(0) lgkmcnt(0)
	s_barrier
	s_mov_b64 s[0:1], s[36:37]
	s_mov_b32 s2, s38
.Lattn_full:
	s_load_dwordx4 s[8:11], s[0:1], 0x0
	s_load_dwordx2 s[14:15], s[0:1], 0x10
	s_lshl_b32 s3, s2, 1
	s_mul_hi_u32 s4, s2, 0xaaaaaaab
	s_and_b32 s3, s3, 14
	s_lshr_b32 s4, s4, 6
	v_add_u32_e32 v1, 0xffffff00, v0
	v_readfirstlane_b32 s16, v0
	s_add_i32 s6, s3, s4
	v_cmp_gt_u32_e32 vcc, 48, v1
	s_and_saveexec_b64 s[12:13], vcc
	s_cbranch_execz .LBB2_2
	s_load_dwordx2 s[4:5], s[0:1], 0x18
	v_mad_u64_u32 v[2:3], s[18:19], s6, 48, v[0:1]
	v_mov_b32_e32 v3, 0
	s_mov_b32 s3, 0xf800000
	s_waitcnt lgkmcnt(0)
	v_lshl_add_u64 v[2:3], v[2:3], 2, s[4:5]
	global_load_dword v1, v[2:3], off offset:-1024
	v_mov_b32_e32 v3, 0x260
	v_mov_b32_e32 v4, 0x20200
	s_waitcnt vmcnt(0)
	v_mul_f32_e32 v2, 0x4f800000, v1
	v_cmp_gt_f32_e32 vcc, s3, v1
	s_nop 1
	v_cndmask_b32_e32 v1, v1, v2, vcc
	v_sqrt_f32_e32 v2, v1
	s_nop 0
	v_add_u32_e32 v5, -1, v2
	v_add_u32_e32 v6, 1, v2
	v_fma_f32 v7, -v5, v2, v1
	v_fma_f32 v8, -v6, v2, v1
	v_cmp_ge_f32_e64 s[4:5], 0, v7
	s_nop 1
	v_cndmask_b32_e64 v2, v2, v5, s[4:5]
	v_cmp_lt_f32_e64 s[4:5], 0, v8
	s_nop 1
	v_cndmask_b32_e64 v2, v2, v6, s[4:5]
	v_mul_f32_e32 v5, 0x37800000, v2
	v_cndmask_b32_e32 v2, v2, v5, vcc
	v_cmp_class_f32_e32 vcc, v1, v3
	s_nop 1
	v_cndmask_b32_e32 v1, v2, v1, vcc
	v_mul_f32_e32 v1, 0x3f800347, v1
	v_lshl_add_u32 v2, v0, 2, v4
	ds_write_b32 v2, v1
